# plus: one static s_setprio 1 for waves 4-7 at kernel entry
# baseline (speedup 1.0000x reference)
.LBB0_5:
	s_or_b64 exec, exec, s[4:5]
	s_lshr_b32 s4, s50, 6
	s_lshl_b32 s2, s94, 3
	v_writelane_b32 v251, s4, 4
	s_cmp_lt_u32 s4, 4
	s_cbranch_scc1 .Lprio_done
	s_setprio 1
.Lprio_done:
	s_add_i32 s33, s4, s2
	s_load_dwordx4 s[4:7], s[90:91], 0xe0
	s_waitcnt lgkmcnt(0)
	s_cmp_lt_i32 s6, 1
	s_cselect_b64 s[4:5], -1, 0
	s_cmp_gt_i32 s7, 0
	s_cselect_b64 s[6:7], -1, 0
	s_and_b64 s[74:75], s[4:5], s[6:7]
	v_cndmask_b32_e64 v0, 0, 1, s[74:75]
	v_cmp_ne_u32_e64 s[6:7], 1, v0
	s_andn2_b64 vcc, exec, s[74:75]
	s_cbranch_vccnz .LBB0_306
	s_and_b32 s2, s50, 0xffffffc0
	v_mbcnt_lo_u32_b32 v186, -1, 0
	v_mbcnt_hi_u32_b32 v186, -1, v186
	s_mov_b64 s[4:5], s[90:91]
	v_add_u32_e32 v0, s2, v186
	s_movk_i32 s2, 0x3fff
	v_cmp_lt_i32_e32 vcc, s2, v0
	s_and_saveexec_b64 s[8:9], vcc
	s_xor_b64 s[8:9], exec, s[8:9]
	s_cbranch_execz .LBB0_8
	s_load_dwordx2 s[10:11], s[4:5], 0x18
	v_and_b32_e32 v1, 0x7ff, v0
	v_lshlrev_b32_e32 v2, 2, v1
	v_mov_b32_e32 v3, 0
	s_waitcnt lgkmcnt(0)
	v_lshl_add_u64 v[2:3], s[10:11], 0, v[2:3]
